# differential attention: static s_setprio 1 for waves 0-3 (component-0 waves, which lead their SIMD partner by one stage), reset before the stick-breaking units
# baseline (speedup 1.0000x reference)
; __device__ __forceinline__ void da_unit(LAS unsigned char* lds, const bf16* __restrict__ Q, const bf16* __restrict__ Kp, const bf16* __restrict__ Vp, const float* __restrict__ gda, float lam, ...
;     constexpr float THR2 = 8.0f * 1.4426950408889634f;
;     const int r32 = lane & 31, hi = lane >> 5, rg = wave & 3, comp = wave >> 2;
;     LAS unsigned char* V_lds = lds; LAS unsigned char* K_lds = lds + 4 * SHM_T; LAS float* X = (LAS float*)lds;
;     LAS float* wsf = (LAS float*)(lds + MISC_OFF + 2048) + wave * 64; LAS float* li_l = wsf; LAS float* al_l = wsf + 32;
;     const int m0 = b * SEQ + 128 * qt;
;     bf16x8 qr[4];
;     { const bf16* Qw = Q + (size_t)(m0 + 32 * rg + r32) * HW + h * 128 + comp * 64 + hi * 8;
; #pragma unroll
;       for (int d0 = 0; d0 < 4; ++d0) qr[d0] = *(const bf16x8*)(Qw + d0 * 16); }
;     const bf16* Kh = Kp + (size_t)(b * LPB) * HW + h * 128; const bf16* Vh = Vp + (size_t)(b * LPB) * HW + h * 128;
;     const int vb0 = (int)(unsigned)(uintptr_t)V_lds + v_rd_base(lane);
;     const int NT = 2 * qt + 3, NTw = 2 * qt + 2 + (rg >> 1);
;     const AttDma dm = att_dma_init(wave, lane);
;     att_dma(dm, Kh, Vh, 0, K_lds, V_lds, wave);
;     att_dma(dm, Kh, Vh, 64, K_lds + SHM_T, V_lds + SHM_T, wave);
;     int kbuf = 0;
;     float m_reg = 0.f, l_reg = 0.f; f32x16 o[4];
;     f32x16 mneg;
; #pragma unroll
;     for (int r = 0; r < 16; ++r) mneg[r] = 0.f;
; #pragma unroll
;     for (int d = 0; d < 4; ++d)
; #pragma unroll
;         for (int r = 0; r < 16; ++r) o[d][r] = 0.f;
;     bf16x8 pa0, pa1, pa2, pa3; bool pend = false; int pbuf = 0, vbuf = 0;
; #pragma unroll
;     for (int q = 0; q < 8; ++q) { pa0[q] = 0; pa1[q] = 0; pa2[q] = 0; pa3[q] = 0; }
; __device__ __forceinline__ void phase_attn(const Args& a, LAS unsigned char* lds, int vcu, int G, int tid, int lane, int wave) {
;     unsigned char* ws = a.ws;
;     const float lam = ((const float*)(ws + WS_CTL))[CW_LAM];
;     for (int idx = vcu; idx < 256; idx += G) {
;         const int s16 = idx & 15;
;         for (int k = 0; k < 4; ++k) { const int bh = ((idx >> 5) << 2) + 2 * (k >> 1) + ((idx >> 4) & 1), b = bh >> 3, h = bh & 7, qt = (k & 1) ? 31 - s16 : s16;
;             att::da_unit(lds, (const bf16*)(ws + WS_DAQ), (const bf16*)(ws + WS_DAK), (const bf16*)(ws + WS_DAV), a.in[I_GDA], lam, (bf16*)(ws + WS_MIX), b, h, qt, tid, wave, lane); }
.LBB0_564:
	s_cmpk_gt_i32 s0, 0xff
	v_lshlrev_b32_e32 v1, 3, v0
	s_waitcnt lgkmcnt(0)
	v_lshrrev_b32_e32 v133, 4, v194
	s_cbranch_scc1 .LBB0_627
	v_readlane_b32 s98, v246, 33
	s_nop 3
	s_cmp_ge_u32 s98, 4
	s_cbranch_scc1 .Lda_prio
	s_setprio 1
.Lda_prio:
	v_mov_b32_e32 v147, 0
	global_load_dword v168, v147, s[92:93] offset:64
	s_add_u32 s2, s92, 0x8200000
	s_addc_u32 s3, s93, 0
	s_add_u32 s61, s92, 0xe400000
	s_addc_u32 s62, s93, 0
	s_add_u32 s63, s92, 0x10500000
	v_readlane_b32 s9, v246, 33
	s_addc_u32 s71, s93, 0
	s_waitcnt vmcnt(23)
	v_bfe_u32 v6, v194, 2, 2
	v_lshrrev_b32_e32 v8, 1, v194
	s_lshl_b32 s53, s9, 2
	v_and_b32_e32 v5, 15, v0
	v_and_or_b32 v6, v8, 8, v6
	v_or_b32_e32 v8, s53, v133
	s_lshl_b32 s54, s9, 1
	v_lshrrev_b32_e32 v164, 5, v194
	v_bitop3_b32 v9, v8, v5, 7 bitop3:0x6c
	v_lshlrev_b32_e32 v8, 11, v8
	s_and_b32 s6, s53, 0x1ffff0
	s_and_b32 s7, s54, 4
	v_lshl_or_b32 v135, v9, 4, v8
	v_or_b32_e32 v8, s54, v164
	s_or_b32 s6, s7, s6
	v_lshlrev_b32_e32 v3, 4, v194
	v_lshlrev_b32_e32 v8, 6, v8
	v_or_b32_e32 v9, s6, v6
	s_add_i32 s6, s9, 8
	v_and_b32_e32 v7, 48, v3
	v_and_b32_e32 v8, 0xc0, v8
	v_lshlrev_b32_e32 v9, 11, v9
	s_lshl_b32 s55, s6, 2
	s_lshl_b32 s56, s6, 1
	v_or3_b32 v137, v9, v8, v7
	v_or_b32_e32 v8, s55, v133
	s_and_b32 s6, s55, 0x1ffff0
	s_and_b32 s7, s56, 4
	v_readlane_b32 s14, v246, 8
	v_lshlrev_b32_e32 v4, 1, v0
	v_bitop3_b32 v9, v8, v5, 7 bitop3:0x6c
	v_lshlrev_b32_e32 v8, 11, v8
	s_or_b32 s6, s7, s6
	s_lshr_b32 s0, s14, 8
	s_lshl_b32 s1, s9, 8
	v_and_b32_e32 v161, 0xc0, v3
	v_and_b32_e32 v162, 32, v4
	v_and_b32_e32 v163, 0x118, v1
	v_lshl_or_b32 v139, v9, 4, v8
	v_or_b32_e32 v8, s56, v164
	v_or_b32_e32 v6, s6, v6
	s_lshl_b32 s6, s9, 10
	s_bfe_u32 s5, s14, 0x20006
	s_add_i32 s74, s1, 0
	s_lshl_b32 s4, s0, 6
	v_lshlrev_b32_e32 v2, 3, v164
	v_or3_b32 v4, v162, v163, v161
	s_bfe_u32 s1, s9, 0x10001
	v_lshlrev_b32_e32 v8, 6, v8
	s_add_i32 s60, 0, 0x10000
	s_add_i32 s57, s6, 0
	s_add_i32 s7, s6, 0x2000
	s_add_i32 s80, 0, 0x14000
	s_add_i32 s74, s74, 0x20800
	s_lshl_b32 s75, s5, 5
	v_and_b32_e32 v8, 0xc0, v8
	v_lshlrev_b32_e32 v6, 11, v6
	s_add_i32 s76, s60, s6
	s_add_i32 s77, s60, s7
	s_add_i32 s58, s57, 0x2000
	s_add_i32 s78, s80, s6
	s_add_i32 s79, s57, 0x4000
	s_add_i32 s80, s80, s7
	s_add_i32 s81, s57, 0x6000
	v_add_u32_e32 v169, 0, v4
	s_or_b32 s82, s1, 2
	v_or_b32_e32 v4, s4, v2
	v_and_b32_e32 v131, 31, v0
	v_or3_b32 v141, v6, v8, v7
	s_cmp_eq_u32 s0, 1
	s_movk_i32 s8, 0x70
	v_mov_b32_e32 v6, 0x2000
	v_lshlrev_b32_e32 v4, 1, v4
	s_cselect_b64 s[12:13], -1, 0
	v_and_b32_e32 v166, 0x70, v3
	v_lshl_or_b32 v170, v194, 8, v6
	v_lshlrev_b32_e32 v6, 2, v131
	s_cmpk_gt_u32 s14, 0xff
	v_bitop3_b32 v173, v4, v3, s8 bitop3:0x78
	v_lshlrev_b32_e32 v3, 11, v164
	s_cselect_b64 s[34:35], -1, 0
	s_cmpk_lt_u32 s14, 0x100
	v_add3_u32 v3, 0, v6, v3
	s_cselect_b64 s[44:45], -1, 0
	v_lshl_add_u32 v177, s5, 14, v3
	s_lshl_b32 s5, s9, 13
	v_add_u32_e32 v172, s60, v170
	s_add_i32 s60, s60, s5
	v_add_u32_e32 v180, s52, v3
	v_or_b32_e32 v3, 4, v133
	v_lshl_add_u32 v149, v3, 8, s60
	v_lshlrev_b32_e32 v132, 11, v3
	v_or_b32_e32 v3, 8, v133
	v_lshl_add_u32 v153, v3, 8, s60
	v_lshlrev_b32_e32 v134, 11, v3
	v_or_b32_e32 v3, 12, v133
	s_add_i32 s84, 0, 0x18000
	v_lshl_add_u32 v154, v3, 8, s60
	v_lshlrev_b32_e32 v136, 11, v3
	v_or_b32_e32 v3, 16, v133
	s_add_i32 s83, s84, s6
	s_movk_i32 s6, 0x60
	v_lshl_add_u32 v155, v3, 8, s60
	v_lshlrev_b32_e32 v138, 11, v3
	v_or_b32_e32 v3, 20, v133
	v_add_u32_e32 v171, s74, v6
	v_bitop3_b32 v174, v4, v166, 32 bitop3:0x36
	v_bitop3_b32 v175, v4, v166, 64 bitop3:0x36
	v_bitop3_b32 v176, v4, v166, s6 bitop3:0x36
	v_lshlrev_b32_e32 v4, 10, v164
	v_lshlrev_b32_e32 v6, 1, v131
	v_lshlrev_b32_e32 v179, 6, v164
	v_lshl_add_u32 v156, v3, 8, s60
	v_lshlrev_b32_e32 v140, 11, v3
	v_or_b32_e32 v3, 24, v133
	v_add3_u32 v178, s60, v4, v6
	v_xor_b32_e32 v4, 64, v179
	v_lshlrev_b32_e32 v143, 4, v5
	v_lshl_add_u32 v157, v3, 8, s60
	v_lshlrev_b32_e32 v142, 11, v3
	v_or_b32_e32 v3, 28, v133
	v_lshlrev_b32_e32 v146, 1, v2
	v_mbcnt_lo_u32_b32 v2, -1, 0
	s_mov_b32 s17, 0
	v_lshlrev_b32_e32 v165, 8, v131
	v_cmp_gt_u32_e64 s[0:1], 32, v194
	v_lshlrev_b32_e32 v167, 4, v164
	s_add_i32 s33, s57, 0x8000
	s_add_i32 s84, s84, s7
	s_add_i32 s59, s57, 0xa000
	v_lshlrev_b32_e32 v148, 3, v5
	v_lshl_add_u32 v145, v133, 8, s60
	v_lshlrev_b32_e32 v130, 11, v133
	v_xor_b32_e32 v152, 64, v143
	v_lshl_add_u32 v158, v3, 8, s60
	v_lshlrev_b32_e32 v144, 11, v3
	s_lshl_b32 s68, s4, 1
	s_mov_b32 s7, 0x20000
	s_brev_b32 s6, -2
	s_mov_b32 s85, 0x40000
	s_mov_b32 s70, 0x3f4ccccd
	v_mov_b32_e32 v181, 0x3727c5ac
	v_add_u32_e32 v159, v178, v4
	v_mbcnt_hi_u32_b32 v160, -1, v2
	v_readlane_b32 s86, v246, 13
	s_branch .LBB0_567

; #define LAS __attribute__((address_space(3)))
; __device__ __forceinline__ int v_rd_base(int lane) { return ((lane & 3) << 3) | (((lane >> 2) & 3) << 6) | (((lane >> 4) & 1) << 5) | (((lane >> 5) & 1) << 8); }
; __device__ __forceinline__ void sb_unit(LAS unsigned char* lds, const bf16* __restrict__ Q, const bf16* __restrict__ Kp, const bf16* __restrict__ Vp, const float* __restrict__ gsb,
;                                         bf16* __restrict__ mixed, int b, int h, int qt, int tid, int wave, int lane) {
;     const int r32 = lane & 31, hi = lane >> 5;
;     LAS unsigned char* V_lds = lds; LAS unsigned char* K_lds = lds + 2 * SHM_T;
;     LAS unsigned* fl = (LAS unsigned*)(lds + MISC_OFF + 4096);
;     const int m0 = b * SEQ + 256 * qt;
;     LAS unsigned char* Qs = lds + 4 * SHM_T + wave * 8192;
;     { const bf16* Qw = Q + (size_t)(m0 + 32 * wave + r32) * HW + h * 128 + hi * 8;
; #pragma unroll
;       for (int d0 = 0; d0 < 8; ++d0) { const bf16x8 qv = *(const bf16x8*)(Qw + d0 * 16); *(LAS bf16x8*)(Qs + KSWZ(r32, (d0 * 16 + hi * 8) * 2)) = qv; } }
;     const bf16* Kh = Kp + (size_t)(b * LPB) * HW + h * 128; const bf16* Vh = Vp + (size_t)(b * LPB) * HW + h * 128;
;     const int vb0 = (int)(unsigned)(uintptr_t)V_lds + v_rd_base(lane);
;     int kb[4];
; #pragma unroll
;     for (int bq = 0; bq < 4; ++bq) kb[bq] = r32 * 256 + ((bq * 32 + hi * 16) ^ ((r32 & 7) << 4));
;     const int jtop = 4 * qt + 4, jw = 4 * qt + 1 + (wave >> 1);
;     const int Prow = 64 + 256 * qt + 32 * wave + r32;
;     if (lane == 0) { fl[wave] = 0u; fl[8 + wave] = 0u; }
;     { const AttDma dm = att_dma_init(wave, lane); att_dma(dm, Kh, Vh, jtop * 64, K_lds, V_lds, wave); }
;     float carry = 0.f; bool done = false; f32x16 o[4];
; #pragma unroll
;     for (int d = 0; d < 4; ++d)
; #pragma unroll
;         for (int r = 0; r < 16; ++r) o[d][r] = 0.f;
; __device__ __forceinline__ void phase_attn(const Args& a, LAS unsigned char* lds, int vcu, int G, int tid, int lane, int wave) {
;     ...
;     for (int idx = vcu; idx < 256; idx += G) {
;         const int bh = idx >> 3, s = idx & 7, b = bh >> 3, h = bh & 7;
;         for (int k = 0; k < 2; ++k)
;             att::sb_unit(lds, (const bf16*)(ws + WS_SBQ), (const bf16*)(ws + WS_SBK), (const bf16*)(ws + WS_SBV), a.in[I_GSB], (bf16*)(ws + WS_MIX), b, h, 2 * s + k, tid, wave, lane);
.LBB0_600:
	s_setprio 0
	v_readlane_b32 s92, v246, 34
	v_readlane_b32 s93, v246, 35
	s_add_u32 s28, s92, 0xa200000
	s_addc_u32 s29, s93, 0
	v_mov_b32_e32 v2, 0
	s_add_u32 s30, s92, 0xc300000
	v_readlane_b32 s2, v246, 33
	v_mov_b32_e32 v147, v2
	s_addc_u32 s31, s93, 0
	s_lshl_b32 s34, s2, 5
	v_lshl_add_u64 v[4:5], s[92:93], 0, v[146:147]
	s_mov_b64 s[2:3], 0x6200000
	v_lshl_add_u64 v[100:101], v[4:5], 0, s[2:3]
	s_movk_i32 s2, 0x60
	v_bitop3_b32 v10, v167, v166, s2 bitop3:0x36
	s_movk_i32 s2, 0x80
	v_bitop3_b32 v11, v167, v166, s2 bitop3:0x36
	s_movk_i32 s2, 0xa0
	v_bitop3_b32 v12, v167, v166, s2 bitop3:0x36
	s_movk_i32 s2, 0xc0
	v_or_b32_e32 v4, 32, v167
	v_or_b32_e32 v5, 64, v167
	v_bitop3_b32 v13, v167, v166, s2 bitop3:0x36
	s_movk_i32 s2, 0xe0
	v_bitop3_b32 v14, v167, v166, s2 bitop3:0x36
	v_bitop3_b32 v116, v4, v165, v166 bitop3:0xde
	v_bitop3_b32 v117, v5, v165, v166 bitop3:0xde
	v_readlane_b32 s2, v246, 8
	v_lshlrev_b32_e32 v4, 1, v148
	v_mov_b32_e32 v5, v2
	s_lshr_b32 s35, s2, 7
	v_lshl_add_u64 v[4:5], s[92:93], 0, v[4:5]
	s_mov_b64 s[6:7], 0x12600000
	v_lshl_add_u64 v[102:103], v[4:5], 0, s[6:7]
	v_or_b32_e32 v4, v161, v163
	s_lshl_b32 s2, s35, 3
	v_add_u32_e32 v3, s60, v165
	v_xor_b32_e32 v6, v167, v166
	v_bitop3_b32 v7, v167, v166, 32 bitop3:0x36
	v_bitop3_b32 v8, v167, v166, 64 bitop3:0x36
	v_or_b32_e32 v9, 0x60, v167
	s_add_i32 s38, s53, 0
	v_lshlrev_b32_e32 v119, 2, v164
	v_add3_u32 v148, v162, 0, v4
	s_sub_i32 s39, s2, 24
	v_or_b32_e32 v4, s34, v131
	v_readlane_b32 s62, v246, 13
	v_readlane_b32 s2, v246, 11
	v_readlane_b32 s94, v246, 36
	v_readlane_b32 s95, v246, 37
	v_bitop3_b32 v115, v167, v165, v166 bitop3:0xde
	v_bitop3_b32 v118, v9, v165, v166 bitop3:0xde
	s_mov_b32 s3, 0
	v_cmp_eq_u32_e64 s[4:5], 0, v194
	s_add_i32 s38, s38, 0x21000
	v_or_b32_e32 v120, 32, v119
	v_or_b32_e32 v121, 33, v119
	v_or_b32_e32 v122, 34, v119
	v_or_b32_e32 v123, 35, v119
	v_or_b32_e32 v124, 40, v119
	v_or_b32_e32 v125, 41, v119
	v_or_b32_e32 v126, 42, v119
	v_or_b32_e32 v127, 43, v119
	v_or_b32_e32 v128, 48, v119
	v_or_b32_e32 v129, 49, v119
	v_or_b32_e32 v146, 50, v119
	v_or_b32_e32 v147, 51, v119
	v_or_b32_e32 v150, 56, v119
	v_or_b32_e32 v151, 57, v119
	v_or_b32_e32 v164, 58, v119
	v_or_b32_e32 v165, 59, v119
	v_or_b32_e32 v166, 1, v119
	v_or_b32_e32 v167, 2, v119
	v_or_b32_e32 v168, 3, v119
	v_or_b32_e32 v169, 8, v119
	v_or_b32_e32 v170, 9, v119
	v_or_b32_e32 v171, 10, v119
	v_or_b32_e32 v172, 11, v119
	v_or_b32_e32 v173, 16, v119
	v_or_b32_e32 v174, 17, v119
	v_or_b32_e32 v175, 18, v119
	v_or_b32_e32 v176, 19, v119
	v_or_b32_e32 v177, 24, v119
	v_or_b32_e32 v178, 25, v119
	v_or_b32_e32 v179, 26, v119
	v_or_b32_e32 v180, 27, v119
	v_add_u32_e32 v161, 0xffffff40, v4
	s_lshl_b32 s44, s62, 1
	s_lshl_b32 s45, s2, 1
	s_mov_b32 s19, 0x20000
	s_brev_b32 s18, -2
	v_add_u32_e32 v162, v3, v6
	v_add_u32_e32 v163, v3, v7
	v_add_u32_e32 v181, v3, v8
	v_add_u32_e32 v182, v3, v10
	v_add_u32_e32 v183, v3, v11
	v_add_u32_e32 v184, v3, v12
	v_add_u32_e32 v185, v3, v13
	v_add_u32_e32 v186, v3, v14
	s_mov_b32 s61, 0xc31b0000
	v_mov_b32_e32 v187, 0x3727c5ac
	v_mov_b32_e32 v188, 0xf149f2ca
	s_branch .LBB0_602

; __global__ void __launch_bounds__(NWAVES * 64, 2) fwd(Args args) {
	.amdhsa_kernel _Z3fwd4Args
		.amdhsa_group_segment_fixed_size 0
		.amdhsa_private_segment_fixed_size 0
		.amdhsa_kernarg_size 432
		.amdhsa_user_sgpr_count 2
		.amdhsa_user_sgpr_dispatch_ptr 0
		.amdhsa_user_sgpr_queue_ptr 0
		.amdhsa_user_sgpr_kernarg_segment_ptr 1
		.amdhsa_user_sgpr_dispatch_id 0
		.amdhsa_user_sgpr_kernarg_preload_length 0
		.amdhsa_user_sgpr_kernarg_preload_offset 0
		.amdhsa_user_sgpr_private_segment_size 0
		.amdhsa_uses_dynamic_stack 0
		.amdhsa_enable_private_segment 0
		.amdhsa_system_sgpr_workgroup_id_x 1
		.amdhsa_system_sgpr_workgroup_id_y 0
		.amdhsa_system_sgpr_workgroup_id_z 0
		.amdhsa_system_sgpr_workgroup_info 0
		.amdhsa_system_vgpr_workitem_id 0
		.amdhsa_next_free_vgpr 247
		.amdhsa_next_free_sgpr 102
		.amdhsa_accum_offset 248
		.amdhsa_reserve_vcc 1
		.amdhsa_float_round_mode_32 0
		.amdhsa_float_round_mode_16_64 0
		.amdhsa_float_denorm_mode_32 3
		.amdhsa_float_denorm_mode_16_64 3
		.amdhsa_dx10_clamp 1
		.amdhsa_ieee_mode 1
		.amdhsa_fp16_overflow 0
		.amdhsa_tg_split 0
		.amdhsa_exception_fp_ieee_invalid_op 0
		.amdhsa_exception_fp_denorm_src 0
		.amdhsa_exception_fp_ieee_div_zero 0
		.amdhsa_exception_fp_ieee_overflow 0
		.amdhsa_exception_fp_ieee_underflow 0
		.amdhsa_exception_fp_ieee_inexact 0
		.amdhsa_exception_int_div_zero 0
	.end_amdhsa_kernel

; __global__ void __launch_bounds__(NWAVES * 64, 2) fwd(Args args) {
amdhsa.kernels:
  - .agpr_count:     0
    .args:
      - .offset:         0
        .size:           176
        .value_kind:     by_value
      - .offset:         176
        .size:           4
        .value_kind:     hidden_block_count_x
      - .offset:         180
        .size:           4
        .value_kind:     hidden_block_count_y
      - .offset:         184
        .size:           4
        .value_kind:     hidden_block_count_z
      - .offset:         188
        .size:           2
        .value_kind:     hidden_group_size_x
      - .offset:         190
        .size:           2
        .value_kind:     hidden_group_size_y
      - .offset:         192
        .size:           2
        .value_kind:     hidden_group_size_z
      - .offset:         194
        .size:           2
        .value_kind:     hidden_remainder_x
      - .offset:         196
        .size:           2
        .value_kind:     hidden_remainder_y
      - .offset:         198
        .size:           2
        .value_kind:     hidden_remainder_z
      - .offset:         216
        .size:           8
        .value_kind:     hidden_global_offset_x
      - .offset:         224
        .size:           8
        .value_kind:     hidden_global_offset_y
      - .offset:         232
        .size:           8
        .value_kind:     hidden_global_offset_z
      - .offset:         240
        .size:           2
        .value_kind:     hidden_grid_dims
      - .offset:         296
        .size:           4
        .value_kind:     hidden_dynamic_lds_size
    .group_segment_fixed_size: 0
    .kernarg_segment_align: 8
    .kernarg_segment_size: 432
    .language:       OpenCL C
    .language_version:
      - 2
      - 0
    .max_flat_workgroup_size: 512
    .name:           _Z3fwd4Args
    .private_segment_fixed_size: 0
    .sgpr_count:     108
    .sgpr_spill_count: 40
    .symbol:         _Z3fwd4Args.kd
    .uniform_work_group_size: 1
    .uses_dynamic_stack: false
    .vgpr_count:     247
    .vgpr_spill_count: 0
    .wavefront_size: 64
